# PV and QK MFMA groups in selected/window/compressed attention wait only for the fragments they use (lgkmcnt 8 then 0), on top of v30
# speedup vs baseline: 1.0190x; 1.0041x over previous
; #define LAS __attribute__((address_space(3)))
; #define TA_SB __builtin_amdgcn_sched_barrier(0)
; __device__ __forceinline__ void ta_ldk(LAS const unsigned char* kb, int kg, int i, int g4, bf16x8 (&a0)[4], bf16x8 (&a1)[4]) {
;     LAS const unsigned char* kr = kb + (32 * kg + 8 * (i >> 2) + (i & 3)) * 256;
; #pragma unroll
;     for (int ks = 0; ks < 4; ++ks) { const int co = ((4 * ks + g4) ^ i) * 16; a0[ks] = *(LAS const bf16x8*)(kr + co); a1[ks] = *(LAS const bf16x8*)(kr + 4 * 256 + co); } }
; __device__ __forceinline__ void ta_ldv(LAS const unsigned char* vb, int kg, int i, int g4, bf16x8 (&vt)[8]) {
;     LAS const unsigned char* vr = vb + i * 128 + (((4 * kg + g4) ^ ((i >> 1) & 7)) * 16);
; #pragma unroll
;     for (int dt = 0; dt < 8; ++dt) vt[dt] = *(LAS const bf16x8*)(vr + dt * 16 * 128); }
; __device__ __forceinline__ void ta_qk(const bf16x8 (&a0)[4], const bf16x8 (&a1)[4], const QF& q, f32x4& s0, f32x4& s1) {
;     s0 = (f32x4){0.f, 0.f, 0.f, 0.f}; s1 = (f32x4){0.f, 0.f, 0.f, 0.f};
; #pragma unroll
;     for (int ks = 0; ks < 4; ++ks) { s0 = __builtin_amdgcn_mfma_f32_16x16x32_bf16(a0[ks], q.f[ks], s0, 0, 0, 0); s1 = __builtin_amdgcn_mfma_f32_16x16x32_bf16(a1[ks], q.f[ks], s1, 0, 0, 0); } }
; template <int MODE, bool FULL = false> __device__ __forceinline__ void ta_compute2(LAS const unsigned char* kb, const QF& q0, const QF& q1, f32x4 (&O0)[8], f32x4 (&O1)[8], float& l0, float& l1, int i, int g4, int tq0, int tq1, bool n0, bool n1, bool cv0, bool cv1, int kbase, float mb, bool full = fa ...
;     LAS const unsigned char* vb = kb + 16384;
;     const float m0 = cv0 ? mb : 1e30f, m1 = cv1 ? mb : 1e30f;
;     bf16x8 ka0[4], ka1[4], kb0[4], kb1[4], va[8], vc[8]; f32x4 s0, s1, t0, t1, u0, u1, v0, v1; bf16x8 pa0, pb0, pa1, pb1;
;     ta_ldk(kb, 0, i, g4, ka0, ka1); ta_ldk(kb, 1, i, g4, kb0, kb1); TA_SB;
;     if (n0) { ta_qk(ka0, ka1, q0, s0, s1); ta_qk(kb0, kb1, q0, t0, t1); } TA_SB;
;     if (n1) { ta_qk(ka0, ka1, q1, u0, u1); ta_qk(kb0, kb1, q1, v0, v1); } TA_SB;
;     ta_ldv(vb, 0, i, g4, va); TA_SB;
.LBB0_438:
	s_and_b32 s0, s48, 0x18000
	s_add_i32 s2, s0, 0
	v_add_u32_e32 v122, s2, v202
	v_add_u32_e32 v134, v122, v203
	v_add_u32_e32 v142, v122, v204
	v_add_u32_e32 v143, v122, v205
	v_add_u32_e32 v144, v122, v206
	ds_read_b128 v[98:101], v134
	ds_read_b128 v[102:105], v134 offset:1024
	ds_read_b128 v[106:109], v142
	ds_read_b128 v[110:113], v142 offset:1024
	ds_read_b128 v[114:117], v143
	ds_read_b128 v[118:121], v143 offset:1024
	ds_read_b128 v[122:125], v144
	ds_read_b128 v[126:129], v144 offset:1024
	ds_read_b128 v[130:133], v134 offset:8192
	ds_read_b128 v[134:137], v134 offset:9216
	ds_read_b128 v[138:141], v142 offset:8192
	ds_read_b128 v[150:153], v142 offset:9216
	ds_read_b128 v[218:221], v143 offset:8192
	ds_read_b128 v[222:225], v143 offset:9216
	ds_read_b128 v[226:229], v144 offset:8192
	ds_read_b128 v[230:233], v144 offset:9216
	s_cmp_ge_i32 s6, s41
	s_cselect_b64 s[0:1], -1, 0
	s_cmp_le_i32 s6, s15
	s_cselect_b64 s[6:7], -1, 0
	s_or_b64 s[16:17], s[0:1], s[6:7]
	s_waitcnt lgkmcnt(8)
	v_mfma_f32_16x16x32_bf16 v[142:145], v[98:101], v[66:69], 0
	v_mfma_f32_16x16x32_bf16 v[146:149], v[102:105], v[66:69], 0
	v_mfma_f32_16x16x32_bf16 v[142:145], v[106:109], v[70:73], v[142:145]
	v_mfma_f32_16x16x32_bf16 v[146:149], v[110:113], v[70:73], v[146:149]
	v_mfma_f32_16x16x32_bf16 v[142:145], v[114:117], v[74:77], v[142:145]
	v_mfma_f32_16x16x32_bf16 v[146:149], v[118:121], v[74:77], v[146:149]
	v_mfma_f32_16x16x32_bf16 v[166:169], v[122:125], v[78:81], v[142:145]
	v_mfma_f32_16x16x32_bf16 v[162:165], v[126:129], v[78:81], v[146:149]
	s_waitcnt lgkmcnt(0)
	v_mfma_f32_16x16x32_bf16 v[142:145], v[130:133], v[66:69], 0
	v_mfma_f32_16x16x32_bf16 v[146:149], v[134:137], v[66:69], 0
	v_mfma_f32_16x16x32_bf16 v[142:145], v[138:141], v[70:73], v[142:145]
	v_mfma_f32_16x16x32_bf16 v[146:149], v[150:153], v[70:73], v[146:149]
	v_mfma_f32_16x16x32_bf16 v[142:145], v[218:221], v[74:77], v[142:145]
	v_mfma_f32_16x16x32_bf16 v[146:149], v[222:225], v[74:77], v[146:149]
	v_mfma_f32_16x16x32_bf16 v[158:161], v[226:229], v[78:81], v[142:145]
	v_mfma_f32_16x16x32_bf16 v[154:157], v[230:233], v[78:81], v[146:149]
	v_mfma_f32_16x16x32_bf16 v[98:101], v[98:101], v[82:85], 0
	v_mfma_f32_16x16x32_bf16 v[102:105], v[102:105], v[82:85], 0
	v_mfma_f32_16x16x32_bf16 v[98:101], v[106:109], v[86:89], v[98:101]
	v_mfma_f32_16x16x32_bf16 v[102:105], v[110:113], v[86:89], v[102:105]
	v_mfma_f32_16x16x32_bf16 v[98:101], v[114:117], v[90:93], v[98:101]
	v_mfma_f32_16x16x32_bf16 v[102:105], v[118:121], v[90:93], v[102:105]
	v_mfma_f32_16x16x32_bf16 v[146:149], v[122:125], v[94:97], v[98:101]
	v_mfma_f32_16x16x32_bf16 v[142:145], v[126:129], v[94:97], v[102:105]
	v_mfma_f32_16x16x32_bf16 v[98:101], v[130:133], v[82:85], 0
	v_mfma_f32_16x16x32_bf16 v[102:105], v[134:137], v[82:85], 0
	v_mfma_f32_16x16x32_bf16 v[98:101], v[138:141], v[86:89], v[98:101]
	v_mfma_f32_16x16x32_bf16 v[102:105], v[150:153], v[86:89], v[102:105]
	v_mfma_f32_16x16x32_bf16 v[98:101], v[218:221], v[90:93], v[98:101]
	v_mfma_f32_16x16x32_bf16 v[102:105], v[222:225], v[90:93], v[102:105]
	v_mfma_f32_16x16x32_bf16 v[138:141], v[226:229], v[94:97], v[98:101]
	v_mfma_f32_16x16x32_bf16 v[134:137], v[230:233], v[94:97], v[102:105]
	v_add_u32_e32 v183, s2, v207
	v_add_u32_e32 v126, v183, v208
	s_nop 2
	ds_read_b128 v[98:101], v126 offset:16384
	ds_read_b128 v[102:105], v126 offset:18432
	ds_read_b128 v[106:109], v126 offset:20480
	ds_read_b128 v[110:113], v126 offset:22528
	ds_read_b128 v[114:117], v126 offset:24576
	ds_read_b128 v[118:121], v126 offset:26624
	ds_read_b128 v[122:125], v126 offset:28672
	ds_read_b128 v[126:129], v126 offset:30720
	s_mov_b64 s[0:1], -1
	s_and_b64 vcc, exec, s[16:17]
	s_cbranch_vccz .LBB0_440
; template <int MODE, bool FULL = false> __device__ __forceinline__ bf16x8 ta_sm(const f32x4 s0, const f32x4 s1, float& l, int kg, int g4, int tq, bool colvalid, int kbase, float mb) {
;     float p[8];
; #pragma unroll
;     for (int r = 0; r < 8; ++r) { const int key = kbase + 32 * kg + 8 * g4 + r; const float sv = r < 4 ? s0[r & 3] : s1[r & 3];
;         bool valid = colvalid && (key <= tq);
;         if (MODE == MODE_WIN) valid = valid && (key > tq - 512);
;         if (MODE == MODE_NONE || FULL) valid = true;
;         p[r] = valid ? __builtin_amdgcn_exp2f(sv * C2_ - mb) : 0.f; }
;     l += ((p[0] + p[1]) + (p[2] + p[3])) + ((p[4] + p[5]) + (p[6] + p[7]));
;     return pack8(p[0], p[1], p[2], p[3], p[4], p[5], p[6], p[7]); }
	v_fma_f32 v133, v164, s38, -v1
	v_exp_f32_e32 v133, v133
	v_subrev_u32_e32 v132, 33, v214
	v_fma_f32 v150, v163, s38, -v1
	v_cmp_le_i32_e32 vcc, v132, v196
	v_cmp_gt_i32_e64 s[6:7], v132, v212
	v_exp_f32_e32 v150, v150
	s_and_b64 vcc, vcc, s[6:7]
	v_subrev_u32_e32 v132, 34, v214
	v_cndmask_b32_e32 v133, 0, v133, vcc
	v_cmp_le_i32_e32 vcc, v132, v196
	v_cmp_gt_i32_e64 s[6:7], v132, v212
	v_fma_f32 v151, v162, s38, -v1
	s_and_b64 vcc, vcc, s[6:7]
	v_exp_f32_e32 v151, v151
	v_cndmask_b32_e32 v132, 0, v150, vcc
	v_subrev_u32_e32 v150, 35, v214
	v_cmp_le_i32_e32 vcc, v150, v196
	v_cmp_gt_i32_e64 s[6:7], v150, v212
	v_fma_f32 v152, v169, s38, -v1
	s_and_b64 vcc, vcc, s[6:7]
	v_exp_f32_e32 v152, v152
	v_cndmask_b32_e32 v150, 0, v151, vcc
	v_subrev_u32_e32 v151, 36, v214
	v_cmp_le_i32_e32 vcc, v151, v196
	v_cmp_gt_i32_e64 s[6:7], v151, v212
	v_fma_f32 v153, v168, s38, -v1
	s_and_b64 vcc, vcc, s[6:7]
	v_exp_f32_e32 v153, v153
	v_cndmask_b32_e32 v151, 0, v152, vcc
	v_subrev_u32_e32 v152, 37, v214
	v_cmp_le_i32_e32 vcc, v152, v196
	v_cmp_gt_i32_e64 s[6:7], v152, v212
	s_and_b64 vcc, vcc, s[6:7]
	v_cndmask_b32_e32 v152, 0, v153, vcc
	v_fma_f32 v153, v167, s38, -v1
	v_exp_f32_e32 v153, v153
	v_subrev_u32_e32 v130, 39, v214
	v_fma_f32 v187, v166, s38, -v1
	v_cmp_lt_i32_e32 vcc, v130, v196
	v_cmp_ge_i32_e64 s[6:7], v130, v212
	v_exp_f32_e32 v187, v187
	s_and_b64 vcc, vcc, s[6:7]
	v_cndmask_b32_e32 v153, 0, v153, vcc
	v_cmp_le_i32_e32 vcc, v130, v196
	v_cmp_gt_i32_e64 s[6:7], v130, v212
	s_and_b64 vcc, vcc, s[6:7]
	v_cndmask_b32_e32 v130, 0, v187, vcc
	v_fma_f32 v187, v165, s38, -v1
	v_exp_f32_e32 v187, v187
	v_subrev_u32_e32 v131, 32, v214
	v_cmp_le_i32_e32 vcc, v131, v196
	v_cmp_gt_i32_e64 s[6:7], v131, v212
	s_and_b64 vcc, vcc, s[6:7]
	v_cndmask_b32_e32 v187, 0, v187, vcc
	v_add_f32_e32 v131, v130, v153
	v_add_f32_e32 v198, v152, v151
	v_add_f32_e32 v131, v131, v198
	v_add_f32_e32 v198, v150, v132
	v_add_f32_e32 v199, v133, v187
	v_add_f32_e32 v198, v198, v199
	v_add_f32_e32 v131, v131, v198
	v_add_f32_e32 v198, v216, v131
	v_cvt_pk_bf16_f32 v130, v130, v153
	v_cvt_pk_bf16_f32 v131, v152, v151
	v_fma_f32 v152, v156, s38, -v1
	v_exp_f32_e32 v152, v152
	v_add_u32_e32 v151, -1, v214
	v_cmp_le_i32_e32 vcc, v151, v196
	v_cmp_gt_i32_e64 s[6:7], v151, v212
	s_and_b64 vcc, vcc, s[6:7]
	v_cndmask_b32_e32 v153, 0, v152, vcc
	v_fma_f32 v152, v155, s38, -v1
	v_exp_f32_e32 v152, v152
	v_cvt_pk_bf16_f32 v132, v150, v132
	v_cvt_pk_bf16_f32 v133, v133, v187
	v_add_u32_e32 v151, -2, v214
	v_fma_f32 v187, v154, s38, -v1
	v_cmp_le_i32_e32 vcc, v151, v196
	v_cmp_gt_i32_e64 s[6:7], v151, v212
	v_exp_f32_e32 v187, v187
	s_and_b64 vcc, vcc, s[6:7]
	v_add_u32_e32 v151, -3, v214
	v_fma_f32 v199, v161, s38, -v1
	v_cndmask_b32_e32 v152, 0, v152, vcc
	v_cmp_le_i32_e32 vcc, v151, v196
	v_cmp_gt_i32_e64 s[6:7], v151, v212
	v_exp_f32_e32 v199, v199
	s_and_b64 vcc, vcc, s[6:7]
	v_add_u32_e32 v151, -4, v214
	v_cndmask_b32_e32 v187, 0, v187, vcc
	v_cmp_le_i32_e32 vcc, v151, v196
	v_cmp_gt_i32_e64 s[6:7], v151, v212
	s_and_b64 vcc, vcc, s[6:7]
	v_fma_f32 v217, v160, s38, -v1
	v_cndmask_b32_e32 v151, 0, v199, vcc
	v_add_u32_e32 v199, -5, v214
	v_exp_f32_e32 v217, v217
	v_cmp_le_i32_e32 vcc, v199, v196
	v_cmp_gt_i32_e64 s[6:7], v199, v212
	v_fma_f32 v199, v159, s38, -v1
	v_exp_f32_e32 v199, v199
	v_add_u32_e32 v150, -7, v214
	s_and_b64 vcc, vcc, s[6:7]
	v_cndmask_b32_e32 v217, 0, v217, vcc
	v_cmp_lt_i32_e32 vcc, v150, v196
	v_cmp_ge_i32_e64 s[6:7], v150, v212
	s_and_b64 vcc, vcc, s[6:7]
	v_cndmask_b32_e32 v218, 0, v199, vcc
	v_fma_f32 v199, v158, s38, -v1
	v_exp_f32_e32 v199, v199
	v_cmp_le_i32_e32 vcc, v150, v196
	v_cmp_gt_i32_e64 s[6:7], v150, v212
	s_and_b64 vcc, vcc, s[6:7]
	v_cndmask_b32_e32 v150, 0, v199, vcc
	v_fma_f32 v199, v157, s38, -v1
	v_exp_f32_e32 v199, v199
	v_cmp_le_i32_e32 vcc, v214, v196
	v_cmp_gt_i32_e64 s[6:7], v214, v212
	s_and_b64 vcc, vcc, s[6:7]
	v_cndmask_b32_e32 v219, 0, v199, vcc
	v_add_f32_e32 v199, v150, v218
	v_add_f32_e32 v220, v217, v151
	v_add_f32_e32 v199, v199, v220
	v_add_f32_e32 v220, v187, v152
	v_add_f32_e32 v221, v153, v219
	v_add_f32_e32 v220, v220, v221
	v_add_f32_e32 v199, v199, v220
	v_add_f32_e32 v199, v198, v199
	v_cvt_pk_bf16_f32 v150, v150, v218
	v_cvt_pk_bf16_f32 v151, v217, v151
	v_cvt_pk_bf16_f32 v152, v187, v152
	v_cvt_pk_bf16_f32 v153, v153, v219
	s_mov_b64 s[0:1], 0

; #define LAS __attribute__((address_space(3)))
; #define TA_SB __builtin_amdgcn_sched_barrier(0)
; __device__ __forceinline__ void ta_ldv(LAS const unsigned char* vb, int kg, int i, int g4, bf16x8 (&vt)[8]) {
;     LAS const unsigned char* vr = vb + i * 128 + (((4 * kg + g4) ^ ((i >> 1) & 7)) * 16);
; #pragma unroll
;     for (int dt = 0; dt < 8; ++dt) vt[dt] = *(LAS const bf16x8*)(vr + dt * 16 * 128); }
; __device__ __forceinline__ void ta_qk(const bf16x8 (&a0)[4], const bf16x8 (&a1)[4], const QF& q, f32x4& s0, f32x4& s1) {
;     s0 = (f32x4){0.f, 0.f, 0.f, 0.f}; s1 = (f32x4){0.f, 0.f, 0.f, 0.f};
; #pragma unroll
;     for (int ks = 0; ks < 4; ++ks) { s0 = __builtin_amdgcn_mfma_f32_16x16x32_bf16(a0[ks], q.f[ks], s0, 0, 0, 0); s1 = __builtin_amdgcn_mfma_f32_16x16x32_bf16(a1[ks], q.f[ks], s1, 0, 0, 0); } }
; template <int MODE, bool FULL = false> __device__ __forceinline__ bf16x8 ta_sm(const f32x4 s0, const f32x4 s1, float& l, int kg, int g4, int tq, bool colvalid, int kbase, float mb) {
;     float p[8];
; #pragma unroll
;     for (int r = 0; r < 8; ++r) { const int key = kbase + 32 * kg + 8 * g4 + r; const float sv = r < 4 ? s0[r & 3] : s1[r & 3];
;         bool valid = colvalid && (key <= tq);
;         if (MODE == MODE_WIN) valid = valid && (key > tq - 512);
;         if (MODE == MODE_NONE || FULL) valid = true;
;         p[r] = valid ? __builtin_amdgcn_exp2f(sv * C2_ - mb) : 0.f; }
;     l += ((p[0] + p[1]) + (p[2] + p[3])) + ((p[4] + p[5]) + (p[6] + p[7]));
;     return pack8(p[0], p[1], p[2], p[3], p[4], p[5], p[6], p[7]); }
; __device__ __forceinline__ void ta_pv(const bf16x8 (&vt)[8], const bf16x8 pf, f32x4 (&O)[8]) {
; #pragma unroll
;     for (int dt = 0; dt < 8; ++dt) O[dt] = __builtin_amdgcn_mfma_f32_16x16x32_bf16(vt[dt], pf, O[dt], 0, 0, 0); }
; template <int MODE, bool FULL = false> __device__ __forceinline__ void ta_compute2(LAS const unsigned char* kb, const QF& q0, const QF& q1, f32x4 (&O0)[8], f32x4 (&O1)[8], float& l0, float& l1, int i, int g4, int tq0, int tq1, bool n0, bool n1, bool cv0, bool cv1, int kbase, float mb, bool full = fa ...
;     ...
;     ta_ldv(vb, 1, i, g4, vc); TA_SB;
;     if (n0) { ta_pv(va, pa0, O0); ta_pv(vc, pb0, O0); } TA_SB;
;     if (n1) { ta_pv(va, pa1, O1); ta_pv(vc, pb1, O1); } TA_SB;
.LBB0_446:
	s_add_i32 s49, s49, 1
	v_add_u32_e32 v183, v183, v209
	ds_read_b128 v[134:137], v183 offset:16384
	ds_read_b128 v[138:141], v183 offset:18432
	ds_read_b128 v[142:145], v183 offset:20480
	ds_read_b128 v[146:149], v183 offset:22528
	ds_read_b128 v[162:165], v183 offset:24576
	ds_read_b128 v[166:169], v183 offset:26624
	ds_read_b128 v[216:219], v183 offset:28672
	ds_read_b128 v[220:223], v183 offset:30720
	s_waitcnt lgkmcnt(8)
	v_mfma_f32_16x16x32_bf16 v[62:65], v[98:101], v[130:133], v[62:65]
	v_mfma_f32_16x16x32_bf16 v[58:61], v[102:105], v[130:133], v[58:61]
	v_mfma_f32_16x16x32_bf16 v[50:53], v[106:109], v[130:133], v[50:53]
	v_mfma_f32_16x16x32_bf16 v[38:41], v[110:113], v[130:133], v[38:41]
	v_mfma_f32_16x16x32_bf16 v[30:33], v[114:117], v[130:133], v[30:33]
	v_mfma_f32_16x16x32_bf16 v[22:25], v[118:121], v[130:133], v[22:25]
	v_mfma_f32_16x16x32_bf16 v[14:17], v[122:125], v[130:133], v[14:17]
	v_mfma_f32_16x16x32_bf16 v[6:9], v[126:129], v[130:133], v[6:9]
	s_waitcnt lgkmcnt(0)
	v_mfma_f32_16x16x32_bf16 v[62:65], v[134:137], v[150:153], v[62:65]
	v_mfma_f32_16x16x32_bf16 v[58:61], v[138:141], v[150:153], v[58:61]
	v_mfma_f32_16x16x32_bf16 v[50:53], v[142:145], v[150:153], v[50:53]
	v_mfma_f32_16x16x32_bf16 v[38:41], v[146:149], v[150:153], v[38:41]
	v_mfma_f32_16x16x32_bf16 v[30:33], v[162:165], v[150:153], v[30:33]
	v_mfma_f32_16x16x32_bf16 v[22:25], v[166:169], v[150:153], v[22:25]
	v_mfma_f32_16x16x32_bf16 v[14:17], v[216:219], v[150:153], v[14:17]
	v_mfma_f32_16x16x32_bf16 v[6:9], v[220:223], v[150:153], v[6:9]
	v_mfma_f32_16x16x32_bf16 v[54:57], v[98:101], v[154:157], v[54:57]
	v_mfma_f32_16x16x32_bf16 v[46:49], v[102:105], v[154:157], v[46:49]
	v_mfma_f32_16x16x32_bf16 v[42:45], v[106:109], v[154:157], v[42:45]
	v_mfma_f32_16x16x32_bf16 v[34:37], v[110:113], v[154:157], v[34:37]
	v_mfma_f32_16x16x32_bf16 v[26:29], v[114:117], v[154:157], v[26:29]
	v_mfma_f32_16x16x32_bf16 v[18:21], v[118:121], v[154:157], v[18:21]
	v_mfma_f32_16x16x32_bf16 v[10:13], v[122:125], v[154:157], v[10:13]
	v_mfma_f32_16x16x32_bf16 v[2:5], v[126:129], v[154:157], v[2:5]
	v_mfma_f32_16x16x32_bf16 v[54:57], v[134:137], v[158:161], v[54:57]
	v_mfma_f32_16x16x32_bf16 v[46:49], v[138:141], v[158:161], v[46:49]
	v_mfma_f32_16x16x32_bf16 v[42:45], v[142:145], v[158:161], v[42:45]
	v_mfma_f32_16x16x32_bf16 v[34:37], v[146:149], v[158:161], v[34:37]
	v_mfma_f32_16x16x32_bf16 v[26:29], v[162:165], v[158:161], v[26:29]
	v_mfma_f32_16x16x32_bf16 v[18:21], v[166:169], v[158:161], v[18:21]
	v_mfma_f32_16x16x32_bf16 v[10:13], v[216:219], v[158:161], v[10:13]
	v_mfma_f32_16x16x32_bf16 v[2:5], v[220:223], v[158:161], v[2:5]
	s_add_i32 s48, s48, 0x8000
	s_add_i32 s0, s47, s49
	s_cmp_eq_u32 s0, 0
	v_add_u32_e32 v214, 64, v214
	s_cbranch_scc1 .LBB0_431
	v_mov_b32_e32 v216, v199
	v_mov_b32_e32 v215, v198
	s_branch .LBB0_434

; #define LAS __attribute__((address_space(3)))
; #define TA_SB __builtin_amdgcn_sched_barrier(0)
; template <int PASS> __device__ __forceinline__ void cmp_compute2(LAS const unsigned char* kb, const QF& q0, const QF& q1, f32x4 (&O0)[8], f32x4 (&O1)[8], float& l0, float& l1, float inv0, float inv1, LAS float* imp0, LAS float* imp1, int i, int g4, int tq0, int tq1, int j, float mb, bool full) {
;     ...
;         ta_ldv(vb, 1, i, g4, vc); TA_SB;
;         ta_pv(va, pa0, O0); ta_pv(vc, pb0, O0); TA_SB;
;         ta_pv(va, pa1, O1); ta_pv(vc, pb1, O1); TA_SB; }
; __device__ __forceinline__ void p4_tiled(const Ctx& C, bool dry = false) {
;     ...
;         for (int n = 0; n < nb; ++n) {
;             asm volatile("s_waitcnt vmcnt(0)" ::: "memory"); __syncthreads();
;             if (n + 1 < nb) ta_issue(lds, (n + 1) & 1, Kbg + (size_t)(n + 1) * 64 * 128, Vbg + (size_t)(n + 1) * 8192, w, lane);
;             LAS const unsigned char* kb = lds + (n & 1) * 32768;
;     ...
;             if (!dry)
;     ...
;             cmp_compute2<2>(kb, q0, q1, O0, O1, l0, l1, mbi0, mbi1, imp0, imp1, i, g4, tq0, tq1, n, mb, 1024 * n + 1039 <= t0);
;         }
.LBB0_561:
	v_add_u32_e32 v225, v236, v222
	ds_read_b128 v[134:137], v225 offset:16384
	ds_read_b128 v[138:141], v225 offset:18432
	ds_read_b128 v[142:145], v225 offset:20480
	ds_read_b128 v[146:149], v225 offset:22528
	ds_read_b128 v[154:157], v225 offset:24576
	ds_read_b128 v[158:161], v225 offset:26624
	ds_read_b128 v[236:239], v225 offset:28672
	ds_read_b128 v[240:243], v225 offset:30720
	s_waitcnt lgkmcnt(8)
	v_mfma_f32_16x16x32_bf16 v[94:97], v[98:101], v[130:133], v[94:97]
	v_mfma_f32_16x16x32_bf16 v[90:93], v[102:105], v[130:133], v[90:93]
	v_mfma_f32_16x16x32_bf16 v[86:89], v[106:109], v[130:133], v[86:89]
	v_mfma_f32_16x16x32_bf16 v[78:81], v[110:113], v[130:133], v[78:81]
	v_mfma_f32_16x16x32_bf16 v[66:69], v[114:117], v[130:133], v[66:69]
	v_mfma_f32_16x16x32_bf16 v[54:57], v[118:121], v[130:133], v[54:57]
	v_mfma_f32_16x16x32_bf16 v[42:45], v[122:125], v[130:133], v[42:45]
	v_mfma_f32_16x16x32_bf16 v[38:41], v[126:129], v[130:133], v[38:41]
	s_waitcnt lgkmcnt(0)
	v_mfma_f32_16x16x32_bf16 v[94:97], v[134:137], v[150:153], v[94:97]
	v_mfma_f32_16x16x32_bf16 v[90:93], v[138:141], v[150:153], v[90:93]
	v_mfma_f32_16x16x32_bf16 v[86:89], v[142:145], v[150:153], v[86:89]
	v_mfma_f32_16x16x32_bf16 v[78:81], v[146:149], v[150:153], v[78:81]
	v_mfma_f32_16x16x32_bf16 v[66:69], v[154:157], v[150:153], v[66:69]
	v_mfma_f32_16x16x32_bf16 v[54:57], v[158:161], v[150:153], v[54:57]
	v_mfma_f32_16x16x32_bf16 v[42:45], v[236:239], v[150:153], v[42:45]
	v_mfma_f32_16x16x32_bf16 v[38:41], v[240:243], v[150:153], v[38:41]
	v_mfma_f32_16x16x32_bf16 v[82:85], v[98:101], v[162:165], v[82:85]
	v_mfma_f32_16x16x32_bf16 v[74:77], v[102:105], v[162:165], v[74:77]
	v_mfma_f32_16x16x32_bf16 v[70:73], v[106:109], v[162:165], v[70:73]
	v_mfma_f32_16x16x32_bf16 v[62:65], v[110:113], v[162:165], v[62:65]
	v_mfma_f32_16x16x32_bf16 v[58:61], v[114:117], v[162:165], v[58:61]
	v_mfma_f32_16x16x32_bf16 v[50:53], v[118:121], v[162:165], v[50:53]
	v_mfma_f32_16x16x32_bf16 v[46:49], v[122:125], v[162:165], v[46:49]
	v_mfma_f32_16x16x32_bf16 v[34:37], v[126:129], v[162:165], v[34:37]
	v_mfma_f32_16x16x32_bf16 v[82:85], v[134:137], v[166:169], v[82:85]
	v_mfma_f32_16x16x32_bf16 v[74:77], v[138:141], v[166:169], v[74:77]
	v_mfma_f32_16x16x32_bf16 v[70:73], v[142:145], v[166:169], v[70:73]
	v_mfma_f32_16x16x32_bf16 v[62:65], v[146:149], v[166:169], v[62:65]
	v_mfma_f32_16x16x32_bf16 v[58:61], v[154:157], v[166:169], v[58:61]
	v_mfma_f32_16x16x32_bf16 v[50:53], v[158:161], v[166:169], v[50:53]
	v_mfma_f32_16x16x32_bf16 v[46:49], v[236:239], v[166:169], v[46:49]
	v_mfma_f32_16x16x32_bf16 v[34:37], v[240:243], v[166:169], v[34:37]
	s_addk_i32 s10, 0x400
	s_add_i32 s11, s11, 0x8000
	s_add_u32 s44, s44, 0x4000
	s_addc_u32 s45, s45, 0
	s_cmp_eq_u32 s7, s2
	v_add_u32_e32 v203, 64, v203
	s_cbranch_scc1 .LBB0_584

; template <int PASS, bool FULL = false> __device__ __forceinline__ bf16x8 cmp_sm(const f32x4 s0, const f32x4 s1, float& l, float mbi  , LAS float* improw, int kg, int i, int g4, int tq, int j, float mb) {
;     float p[8];
; #pragma unroll
;     for (int r = 0; r < 8; ++r) { const int key = 64 * j + 32 * kg + 8 * g4 + r; const float sv = r < 4 ? s0[r & 3] : s1[r & 3];
; template <int PASS> __device__ __forceinline__ void cmp_compute2(LAS const unsigned char* kb, const QF& q0, const QF& q1, f32x4 (&O0)[8], f32x4 (&O1)[8], float& l0, float& l1, float inv0, float inv1, LAS float* imp0, LAS float* imp1, int i, int g4, int tq0, int tq1, int j, float mb, bool full) {
;     LAS const unsigned char* vb = kb + 16384;
;     bf16x8 ka0[4], ka1[4], kb0[4], kb1[4]; f32x4 s0, s1, t0, t1, u0, u1, v0, v1;
;     ta_ldk(kb, 0, i, g4, ka0, ka1); ta_ldk(kb, 1, i, g4, kb0, kb1); TA_SB;
;     ta_qk(ka0, ka1, q0, s0, s1); ta_qk(kb0, kb1, q0, t0, t1); TA_SB;
;     ta_qk(ka0, ka1, q1, u0, u1); ta_qk(kb0, kb1, q1, v0, v1); TA_SB;
;     if (PASS == 1) {
;         if (full) { (void)cmp_sm<1, true>(s0, s1, l0, inv0, imp0, 0, i, g4, tq0, j, mb); (void)cmp_sm<1, true>(t0, t1, l0, inv0, imp0, 1, i, g4, tq0, j, mb);
;                     (void)cmp_sm<1, true>(u0, u1, l1, inv1, imp1, 0, i, g4, tq1, j, mb); (void)cmp_sm<1, true>(v0, v1, l1, inv1, imp1, 1, i, g4, tq1, j, mb); }
;         else { (void)cmp_sm<1>(s0, s1, l0, inv0, imp0, 0, i, g4, tq0, j, mb); (void)cmp_sm<1>(t0, t1, l0, inv0, imp0, 1, i, g4, tq0, j, mb);
;                (void)cmp_sm<1>(u0, u1, l1, inv1, imp1, 0, i, g4, tq1, j, mb); (void)cmp_sm<1>(v0, v1, l1, inv1, imp1, 1, i, g4, tq1, j, mb); }
;         TA_SB; }
;     else { bf16x8 va[8], vc[8], pa0, pb0, pa1, pb1;
;         ta_ldv(vb, 0, i, g4, va); TA_SB;
;         if (full) { pa0 = cmp_sm<2, true>(s0, s1, l0, inv0, imp0, 0, i, g4, tq0, j, mb); pb0 = cmp_sm<2, true>(t0, t1, l0, inv0, imp0, 1, i, g4, tq0, j, mb);
;                     pa1 = cmp_sm<2, true>(u0, u1, l1, inv1, imp1, 0, i, g4, tq1, j, mb); pb1 = cmp_sm<2, true>(v0, v1, l1, inv1, imp1, 1, i, g4, tq1, j, mb); }
;         else { pa0 = cmp_sm<2>(s0, s1, l0, inv0, imp0, 0, i, g4, tq0, j, mb); pb0 = cmp_sm<2>(t0, t1, l0, inv0, imp0, 1, i, g4, tq0, j, mb);
;                pa1 = cmp_sm<2>(u0, u1, l1, inv1, imp1, 0, i, g4, tq1, j, mb); pb1 = cmp_sm<2>(v0, v1, l1, inv1, imp1, 1, i, g4, tq1, j, mb); }
;         TA_SB;
.LBB0_564:
	s_add_i32 s0, s11, 0xffff8000
	s_and_b32 s0, s0, 0x8000
	s_add_i32 s0, s0, 0
	v_add_u32_e32 v122, s0, v214
	v_add_u32_e32 v134, v122, v215
	v_add_u32_e32 v142, v122, v216
	v_add_u32_e32 v143, v122, v217
	v_add_u32_e32 v144, v122, v218
	ds_read_b128 v[98:101], v134
	ds_read_b128 v[102:105], v134 offset:1024
	ds_read_b128 v[106:109], v142
	ds_read_b128 v[110:113], v142 offset:1024
	ds_read_b128 v[114:117], v143
	ds_read_b128 v[118:121], v143 offset:1024
	ds_read_b128 v[122:125], v144
	ds_read_b128 v[126:129], v144 offset:1024
	ds_read_b128 v[130:133], v134 offset:8192
	ds_read_b128 v[134:137], v134 offset:9216
	ds_read_b128 v[138:141], v142 offset:8192
	ds_read_b128 v[150:153], v142 offset:9216
	ds_read_b128 v[162:165], v143 offset:8192
	ds_read_b128 v[166:169], v143 offset:9216
	ds_read_b128 v[236:239], v144 offset:8192
	ds_read_b128 v[240:243], v144 offset:9216
	s_cmp_gt_i32 s10, s5
	s_waitcnt lgkmcnt(8)
	v_mfma_f32_16x16x32_bf16 v[142:145], v[98:101], v[2:5], 0
	v_mfma_f32_16x16x32_bf16 v[146:149], v[102:105], v[2:5], 0
	v_mfma_f32_16x16x32_bf16 v[142:145], v[106:109], v[6:9], v[142:145]
	v_mfma_f32_16x16x32_bf16 v[146:149], v[110:113], v[6:9], v[146:149]
	v_mfma_f32_16x16x32_bf16 v[142:145], v[114:117], v[10:13], v[142:145]
	v_mfma_f32_16x16x32_bf16 v[146:149], v[118:121], v[10:13], v[146:149]
	v_mfma_f32_16x16x32_bf16 v[244:247], v[122:125], v[14:17], v[142:145]
	v_mfma_f32_16x16x32_bf16 v[248:251], v[126:129], v[14:17], v[146:149]
	s_waitcnt lgkmcnt(0)
	v_mfma_f32_16x16x32_bf16 v[142:145], v[130:133], v[2:5], 0
	v_mfma_f32_16x16x32_bf16 v[146:149], v[134:137], v[2:5], 0
	v_mfma_f32_16x16x32_bf16 v[142:145], v[138:141], v[6:9], v[142:145]
	v_mfma_f32_16x16x32_bf16 v[146:149], v[150:153], v[6:9], v[146:149]
	v_mfma_f32_16x16x32_bf16 v[142:145], v[162:165], v[10:13], v[142:145]
	v_mfma_f32_16x16x32_bf16 v[146:149], v[166:169], v[10:13], v[146:149]
	v_mfma_f32_16x16x32_bf16 v[158:161], v[236:239], v[14:17], v[142:145]
	v_mfma_f32_16x16x32_bf16 v[154:157], v[240:243], v[14:17], v[146:149]
	v_mfma_f32_16x16x32_bf16 v[98:101], v[98:101], v[18:21], 0
	v_mfma_f32_16x16x32_bf16 v[102:105], v[102:105], v[18:21], 0
	v_mfma_f32_16x16x32_bf16 v[98:101], v[106:109], v[22:25], v[98:101]
	v_mfma_f32_16x16x32_bf16 v[102:105], v[110:113], v[22:25], v[102:105]
	v_mfma_f32_16x16x32_bf16 v[98:101], v[114:117], v[26:29], v[98:101]
	v_mfma_f32_16x16x32_bf16 v[102:105], v[118:121], v[26:29], v[102:105]
	v_mfma_f32_16x16x32_bf16 v[146:149], v[122:125], v[30:33], v[98:101]
	v_mfma_f32_16x16x32_bf16 v[142:145], v[126:129], v[30:33], v[102:105]
	v_mfma_f32_16x16x32_bf16 v[98:101], v[130:133], v[18:21], 0
	v_mfma_f32_16x16x32_bf16 v[102:105], v[134:137], v[18:21], 0
	v_mfma_f32_16x16x32_bf16 v[98:101], v[138:141], v[22:25], v[98:101]
	v_mfma_f32_16x16x32_bf16 v[102:105], v[150:153], v[22:25], v[102:105]
	v_mfma_f32_16x16x32_bf16 v[98:101], v[162:165], v[26:29], v[98:101]
	v_mfma_f32_16x16x32_bf16 v[102:105], v[166:169], v[26:29], v[102:105]
	v_mfma_f32_16x16x32_bf16 v[138:141], v[236:239], v[30:33], v[98:101]
	v_mfma_f32_16x16x32_bf16 v[134:137], v[240:243], v[30:33], v[102:105]
	v_add_u32_e32 v236, s0, v220
	v_add_u32_e32 v126, v236, v221
	s_nop 2
	ds_read_b128 v[98:101], v126 offset:16384
	ds_read_b128 v[102:105], v126 offset:18432
	ds_read_b128 v[106:109], v126 offset:20480
	ds_read_b128 v[110:113], v126 offset:22528
	ds_read_b128 v[114:117], v126 offset:24576
	ds_read_b128 v[118:121], v126 offset:26624
	ds_read_b128 v[122:125], v126 offset:28672
	ds_read_b128 v[126:129], v126 offset:30720
	s_mov_b64 s[0:1], -1
	v_fma_f32 v244, v244, s55, -v199
	v_fma_f32 v243, v245, s55, -v199
	v_fma_f32 v242, v246, s55, -v199
	v_fma_f32 v241, v247, s55, -v199
	v_fma_f32 v240, v248, s55, -v199
	v_fma_f32 v239, v249, s55, -v199
	v_fma_f32 v238, v250, s55, -v199
	v_fma_f32 v237, v251, s55, -v199
	s_cbranch_scc1 .LBB0_574
	v_exp_f32_e32 v132, v240
	v_exp_f32_e32 v151, v239
	v_exp_f32_e32 v130, v244
	v_exp_f32_e32 v153, v243
	v_exp_f32_e32 v133, v238
	v_exp_f32_e32 v131, v242
	v_exp_f32_e32 v152, v241
	v_exp_f32_e32 v150, v237
	v_add_f32_e32 v163, v132, v151
	v_add_f32_e32 v162, v130, v153
	v_add_f32_e32 v163, v133, v163
	v_add_f32_e32 v162, v131, v162
	v_fma_f32 v163, 2.0, v163, v152
	v_fma_f32 v162, 2.0, v162, v152
	v_add_f32_e32 v164, v150, v163
	v_add_f32_dpp v166, v150, v150 quad_perm:[1,0,3,2] row_mask:0xf bank_mask:0xf bound_ctrl:1
	v_add_f32_dpp v162, v162, v162 quad_perm:[1,0,3,2] row_mask:0xf bank_mask:0xf bound_ctrl:1
	v_add_f32_dpp v164, v164, v164 quad_perm:[1,0,3,2] row_mask:0xf bank_mask:0xf bound_ctrl:1
	v_mov_b32_dpp v167, v166 quad_perm:[2,3,0,1] row_mask:0xf bank_mask:0xf bound_ctrl:1
	v_mov_b32_dpp v163, v162 quad_perm:[2,3,0,1] row_mask:0xf bank_mask:0xf bound_ctrl:1
	v_mov_b32_dpp v165, v164 quad_perm:[2,3,0,1] row_mask:0xf bank_mask:0xf bound_ctrl:1
	s_and_saveexec_b64 s[0:1], s[8:9]
	s_cbranch_execz .LBB0_567
	v_add_f32_e32 v162, v162, v163
	v_add_f32_e32 v163, v164, v165
	v_add_f32_e32 v164, v166, v167
	s_waitcnt vmcnt(0)
	ds_add_f32 v203, v162
	ds_add_f32 v203, v163 offset:4
	ds_add_f32 v203, v164 offset:8

; #define LAS __attribute__((address_space(3)))
; #define TA_SB __builtin_amdgcn_sched_barrier(0)
; __device__ __forceinline__ void ta_ldv(LAS const unsigned char* vb, int kg, int i, int g4, bf16x8 (&vt)[8]) {
;     LAS const unsigned char* vr = vb + i * 128 + (((4 * kg + g4) ^ ((i >> 1) & 7)) * 16);
; #pragma unroll
;     for (int dt = 0; dt < 8; ++dt) vt[dt] = *(LAS const bf16x8*)(vr + dt * 16 * 128); }
; __device__ __forceinline__ void ta_qk(const bf16x8 (&a0)[4], const bf16x8 (&a1)[4], const QF& q, f32x4& s0, f32x4& s1) {
;     s0 = (f32x4){0.f, 0.f, 0.f, 0.f}; s1 = (f32x4){0.f, 0.f, 0.f, 0.f};
; #pragma unroll
;     for (int ks = 0; ks < 4; ++ks) { s0 = __builtin_amdgcn_mfma_f32_16x16x32_bf16(a0[ks], q.f[ks], s0, 0, 0, 0); s1 = __builtin_amdgcn_mfma_f32_16x16x32_bf16(a1[ks], q.f[ks], s1, 0, 0, 0); } }
; template <int MODE, bool FULL = false> __device__ __forceinline__ bf16x8 ta_sm(const f32x4 s0, const f32x4 s1, float& l, int kg, int g4, int tq, bool colvalid, int kbase, float mb) {
;     float p[8];
; #pragma unroll
;     for (int r = 0; r < 8; ++r) { const int key = kbase + 32 * kg + 8 * g4 + r; const float sv = r < 4 ? s0[r & 3] : s1[r & 3];
;         bool valid = colvalid && (key <= tq);
;         if (MODE == MODE_WIN) valid = valid && (key > tq - 512);
;         if (MODE == MODE_NONE || FULL) valid = true;
;         p[r] = valid ? __builtin_amdgcn_exp2f(sv * C2_ - mb) : 0.f; }
;     l += ((p[0] + p[1]) + (p[2] + p[3])) + ((p[4] + p[5]) + (p[6] + p[7]));
;     return pack8(p[0], p[1], p[2], p[3], p[4], p[5], p[6], p[7]); }
; __device__ __forceinline__ void ta_pv(const bf16x8 (&vt)[8], const bf16x8 pf, f32x4 (&O)[8]) {
; #pragma unroll
;     for (int dt = 0; dt < 8; ++dt) O[dt] = __builtin_amdgcn_mfma_f32_16x16x32_bf16(vt[dt], pf, O[dt], 0, 0, 0); }
; template <int MODE, bool FULL = false> __device__ __forceinline__ void ta_compute2(LAS const unsigned char* kb, const QF& q0, const QF& q1, f32x4 (&O0)[8], f32x4 (&O1)[8], float& l0, float& l1, int i, int g4, int tq0, int tq1, bool n0, bool n1, bool cv0, bool cv1, int kbase, float mb, bool full = fa ...
;     ...
;     ta_ldv(vb, 1, i, g4, vc); TA_SB;
;     if (n0) { ta_pv(va, pa0, O0); ta_pv(vc, pb0, O0); } TA_SB;
;     if (n1) { ta_pv(va, pa1, O1); ta_pv(vc, pb1, O1); } TA_SB;
.LBB0_717:
.LBB0_718:
	v_add_u32_e32 v174, v170, v241
	ds_read_b128 v[130:133], v174 offset:16384
	ds_read_b128 v[134:137], v174 offset:18432
	ds_read_b128 v[138:141], v174 offset:20480
	ds_read_b128 v[142:145], v174 offset:22528
	ds_read_b128 v[162:165], v174 offset:24576
	ds_read_b128 v[166:169], v174 offset:26624
	ds_read_b128 v[170:173], v174 offset:28672
	ds_read_b128 v[174:177], v174 offset:30720
	s_and_b64 vcc, exec, s[14:15]
	s_cbranch_vccnz .LBB0_720
	s_waitcnt lgkmcnt(8)
	v_mfma_f32_16x16x32_bf16 v[62:65], v[98:101], v[146:149], v[62:65]
	v_mfma_f32_16x16x32_bf16 v[58:61], v[102:105], v[146:149], v[58:61]
	v_mfma_f32_16x16x32_bf16 v[46:49], v[106:109], v[146:149], v[46:49]
	v_mfma_f32_16x16x32_bf16 v[38:41], v[110:113], v[146:149], v[38:41]
	v_mfma_f32_16x16x32_bf16 v[30:33], v[114:117], v[146:149], v[30:33]
	v_mfma_f32_16x16x32_bf16 v[22:25], v[118:121], v[146:149], v[22:25]
	v_mfma_f32_16x16x32_bf16 v[14:17], v[122:125], v[146:149], v[14:17]
	v_mfma_f32_16x16x32_bf16 v[6:9], v[126:129], v[146:149], v[6:9]
	s_waitcnt lgkmcnt(0)
	v_mfma_f32_16x16x32_bf16 v[62:65], v[130:133], v[150:153], v[62:65]
	v_mfma_f32_16x16x32_bf16 v[58:61], v[134:137], v[150:153], v[58:61]
	v_mfma_f32_16x16x32_bf16 v[46:49], v[138:141], v[150:153], v[46:49]
	v_mfma_f32_16x16x32_bf16 v[38:41], v[142:145], v[150:153], v[38:41]
	v_mfma_f32_16x16x32_bf16 v[30:33], v[162:165], v[150:153], v[30:33]
	v_mfma_f32_16x16x32_bf16 v[22:25], v[166:169], v[150:153], v[22:25]
	v_mfma_f32_16x16x32_bf16 v[14:17], v[170:173], v[150:153], v[14:17]
	v_mfma_f32_16x16x32_bf16 v[6:9], v[174:177], v[150:153], v[6:9]
.LBB0_720:
	s_and_b64 vcc, exec, s[16:17]
	s_cbranch_vccnz .LBB0_722
	s_waitcnt lgkmcnt(8)
	v_mfma_f32_16x16x32_bf16 v[54:57], v[98:101], v[154:157], v[54:57]
	v_mfma_f32_16x16x32_bf16 v[50:53], v[102:105], v[154:157], v[50:53]
	v_mfma_f32_16x16x32_bf16 v[42:45], v[106:109], v[154:157], v[42:45]
	v_mfma_f32_16x16x32_bf16 v[34:37], v[110:113], v[154:157], v[34:37]
	v_mfma_f32_16x16x32_bf16 v[26:29], v[114:117], v[154:157], v[26:29]
	v_mfma_f32_16x16x32_bf16 v[18:21], v[118:121], v[154:157], v[18:21]
	v_mfma_f32_16x16x32_bf16 v[10:13], v[122:125], v[154:157], v[10:13]
	v_mfma_f32_16x16x32_bf16 v[2:5], v[126:129], v[154:157], v[2:5]
	s_waitcnt lgkmcnt(0)
	v_mfma_f32_16x16x32_bf16 v[54:57], v[130:133], v[158:161], v[54:57]
	v_mfma_f32_16x16x32_bf16 v[50:53], v[134:137], v[158:161], v[50:53]
	v_mfma_f32_16x16x32_bf16 v[42:45], v[138:141], v[158:161], v[42:45]
	v_mfma_f32_16x16x32_bf16 v[34:37], v[142:145], v[158:161], v[34:37]
	v_mfma_f32_16x16x32_bf16 v[26:29], v[162:165], v[158:161], v[26:29]
	v_mfma_f32_16x16x32_bf16 v[18:21], v[166:169], v[158:161], v[18:21]
	v_mfma_f32_16x16x32_bf16 v[10:13], v[170:173], v[158:161], v[10:13]
	v_mfma_f32_16x16x32_bf16 v[2:5], v[174:177], v[158:161], v[2:5]

; #define LAS __attribute__((address_space(3)))
; #define TA_SB __builtin_amdgcn_sched_barrier(0)
; __device__ __forceinline__ void ta_ldv(LAS const unsigned char* vb, int kg, int i, int g4, bf16x8 (&vt)[8]) {
;     LAS const unsigned char* vr = vb + i * 128 + (((4 * kg + g4) ^ ((i >> 1) & 7)) * 16);
; #pragma unroll
;     for (int dt = 0; dt < 8; ++dt) vt[dt] = *(LAS const bf16x8*)(vr + dt * 16 * 128); }
; __device__ __forceinline__ void ta_qk(const bf16x8 (&a0)[4], const bf16x8 (&a1)[4], const QF& q, f32x4& s0, f32x4& s1) {
;     s0 = (f32x4){0.f, 0.f, 0.f, 0.f}; s1 = (f32x4){0.f, 0.f, 0.f, 0.f};
; #pragma unroll
;     for (int ks = 0; ks < 4; ++ks) { s0 = __builtin_amdgcn_mfma_f32_16x16x32_bf16(a0[ks], q.f[ks], s0, 0, 0, 0); s1 = __builtin_amdgcn_mfma_f32_16x16x32_bf16(a1[ks], q.f[ks], s1, 0, 0, 0); } }
; template <int MODE, bool FULL = false> __device__ __forceinline__ bf16x8 ta_sm(const f32x4 s0, const f32x4 s1, float& l, int kg, int g4, int tq, bool colvalid, int kbase, float mb) {
;     float p[8];
; #pragma unroll
;     for (int r = 0; r < 8; ++r) { const int key = kbase + 32 * kg + 8 * g4 + r; const float sv = r < 4 ? s0[r & 3] : s1[r & 3];
;         bool valid = colvalid && (key <= tq);
;         if (MODE == MODE_WIN) valid = valid && (key > tq - 512);
;         if (MODE == MODE_NONE || FULL) valid = true;
;         p[r] = valid ? __builtin_amdgcn_exp2f(sv * C2_ - mb) : 0.f; }
;     l += ((p[0] + p[1]) + (p[2] + p[3])) + ((p[4] + p[5]) + (p[6] + p[7]));
;     return pack8(p[0], p[1], p[2], p[3], p[4], p[5], p[6], p[7]); }
; __device__ __forceinline__ void ta_pv(const bf16x8 (&vt)[8], const bf16x8 pf, f32x4 (&O)[8]) {
; #pragma unroll
;     for (int dt = 0; dt < 8; ++dt) O[dt] = __builtin_amdgcn_mfma_f32_16x16x32_bf16(vt[dt], pf, O[dt], 0, 0, 0); }
; template <int MODE, bool FULL = false> __device__ __forceinline__ void ta_compute2(LAS const unsigned char* kb, const QF& q0, const QF& q1, f32x4 (&O0)[8], f32x4 (&O1)[8], float& l0, float& l1, int i, int g4, int tq0, int tq1, bool n0, bool n1, bool cv0, bool cv1, int kbase, float mb, bool full = fa ...
;     ...
;     ta_ldv(vb, 1, i, g4, vc); TA_SB;
;     if (n0) { ta_pv(va, pa0, O0); ta_pv(vc, pb0, O0); } TA_SB;
;     if (n1) { ta_pv(va, pa1, O1); ta_pv(vc, pb1, O1); } TA_SB;
.LBB0_742:
.LBB0_743:
	v_add_u32_e32 v174, v170, v241
	ds_read_b128 v[130:133], v174 offset:16384
	ds_read_b128 v[138:141], v174 offset:18432
	ds_read_b128 v[142:145], v174 offset:20480
	ds_read_b128 v[146:149], v174 offset:22528
	ds_read_b128 v[162:165], v174 offset:24576
	ds_read_b128 v[166:169], v174 offset:26624
	ds_read_b128 v[170:173], v174 offset:28672
	ds_read_b128 v[174:177], v174 offset:30720
	s_and_b64 vcc, exec, s[14:15]
	s_cbranch_vccnz .LBB0_745
	s_waitcnt lgkmcnt(8)
	v_mfma_f32_16x16x32_bf16 v[62:65], v[98:101], v[134:137], v[62:65]
	v_mfma_f32_16x16x32_bf16 v[58:61], v[102:105], v[134:137], v[58:61]
	v_mfma_f32_16x16x32_bf16 v[46:49], v[106:109], v[134:137], v[46:49]
	v_mfma_f32_16x16x32_bf16 v[38:41], v[110:113], v[134:137], v[38:41]
	v_mfma_f32_16x16x32_bf16 v[30:33], v[114:117], v[134:137], v[30:33]
	v_mfma_f32_16x16x32_bf16 v[22:25], v[118:121], v[134:137], v[22:25]
	v_mfma_f32_16x16x32_bf16 v[14:17], v[122:125], v[134:137], v[14:17]
	v_mfma_f32_16x16x32_bf16 v[6:9], v[126:129], v[134:137], v[6:9]
	s_waitcnt lgkmcnt(0)
	v_mfma_f32_16x16x32_bf16 v[62:65], v[130:133], v[150:153], v[62:65]
	v_mfma_f32_16x16x32_bf16 v[58:61], v[138:141], v[150:153], v[58:61]
	v_mfma_f32_16x16x32_bf16 v[46:49], v[142:145], v[150:153], v[46:49]
	v_mfma_f32_16x16x32_bf16 v[38:41], v[146:149], v[150:153], v[38:41]
	v_mfma_f32_16x16x32_bf16 v[30:33], v[162:165], v[150:153], v[30:33]
	v_mfma_f32_16x16x32_bf16 v[22:25], v[166:169], v[150:153], v[22:25]
	v_mfma_f32_16x16x32_bf16 v[14:17], v[170:173], v[150:153], v[14:17]
	v_mfma_f32_16x16x32_bf16 v[6:9], v[174:177], v[150:153], v[6:9]
.LBB0_745:
	s_and_b64 vcc, exec, s[16:17]
	s_cbranch_vccnz .LBB0_747
	s_waitcnt lgkmcnt(8)
	v_mfma_f32_16x16x32_bf16 v[54:57], v[98:101], v[154:157], v[54:57]
	v_mfma_f32_16x16x32_bf16 v[50:53], v[102:105], v[154:157], v[50:53]
	v_mfma_f32_16x16x32_bf16 v[42:45], v[106:109], v[154:157], v[42:45]
	v_mfma_f32_16x16x32_bf16 v[34:37], v[110:113], v[154:157], v[34:37]
	v_mfma_f32_16x16x32_bf16 v[26:29], v[114:117], v[154:157], v[26:29]
	v_mfma_f32_16x16x32_bf16 v[18:21], v[118:121], v[154:157], v[18:21]
	v_mfma_f32_16x16x32_bf16 v[10:13], v[122:125], v[154:157], v[10:13]
	v_mfma_f32_16x16x32_bf16 v[2:5], v[126:129], v[154:157], v[2:5]
	s_waitcnt lgkmcnt(0)
	v_mfma_f32_16x16x32_bf16 v[54:57], v[130:133], v[158:161], v[54:57]
	v_mfma_f32_16x16x32_bf16 v[50:53], v[138:141], v[158:161], v[50:53]
	v_mfma_f32_16x16x32_bf16 v[42:45], v[142:145], v[158:161], v[42:45]
	v_mfma_f32_16x16x32_bf16 v[34:37], v[146:149], v[158:161], v[34:37]
	v_mfma_f32_16x16x32_bf16 v[26:29], v[162:165], v[158:161], v[26:29]
	v_mfma_f32_16x16x32_bf16 v[18:21], v[166:169], v[158:161], v[18:21]
	v_mfma_f32_16x16x32_bf16 v[10:13], v[170:173], v[158:161], v[10:13]
	v_mfma_f32_16x16x32_bf16 v[2:5], v[174:177], v[158:161], v[2:5]
